# HGRN2 chunk loop: the four serialized LDS read->scale->write round trips after the second barrier now issue all four ds_read_b128 up front (into dead v34-v45) with counted lgkmcnt waits
# speedup vs baseline: 1.0097x; 1.0097x over previous
.LBB0_302:
	v_lshlrev_b32_e32 v139, 2, v101
	v_add_u32_e32 v6, s26, v139
	v_lshl_add_u32 v2, v6, 2, 0
	v_add_u32_e32 v7, 0x10400, v2
	s_waitcnt lgkmcnt(0)
	s_barrier
	ds_read_b128 v[2:5], v7
	ds_read_b128 v[34:37], v7 offset:32
	ds_read_b128 v[38:41], v7 offset:64
	ds_read_b128 v[42:45], v7 offset:96
	v_lshlrev_b32_e32 v8, 4, v100
	v_and_b32_e32 v9, 0xf0, v8
	v_lshl_add_u32 v10, v100, 8, s27
	v_lshlrev_b32_e32 v6, 1, v6
	s_waitcnt lgkmcnt(3)
	v_mul_f32_e32 v2, v84, v2
	v_mul_f32_e32 v3, v85, v3
	v_cvt_pk_bf16_f32 v2, v2, v3
	v_mul_f32_e32 v3, v86, v4
	v_mul_f32_e32 v4, v87, v5
	v_cvt_pk_bf16_f32 v3, v3, v4
	v_xad_u32 v4, v6, v9, v10
	ds_write_b64 v4, v[2:3] offset:32768
	s_waitcnt lgkmcnt(3)
	v_mul_f32_e32 v2, v88, v34
	v_mul_f32_e32 v3, v89, v35
	v_cvt_pk_bf16_f32 v2, v2, v3
	v_mul_f32_e32 v3, v90, v36
	v_mul_f32_e32 v4, v91, v37
	v_cvt_pk_bf16_f32 v3, v3, v4
	v_add_u32_e32 v4, 16, v6
	v_xad_u32 v4, v4, v9, v10
	ds_write_b64 v4, v[2:3] offset:32768
	s_waitcnt lgkmcnt(3)
	v_mul_f32_e32 v2, v92, v38
	v_mul_f32_e32 v3, v93, v39
	v_cvt_pk_bf16_f32 v2, v2, v3
	v_mul_f32_e32 v3, v94, v40
	v_mul_f32_e32 v4, v95, v41
	v_cvt_pk_bf16_f32 v3, v3, v4
	v_add_u32_e32 v4, 32, v6
	v_xad_u32 v4, v4, v9, v10
	ds_write_b64 v4, v[2:3] offset:32768
	s_waitcnt lgkmcnt(3)
	v_mul_f32_e32 v2, v96, v42
	v_mul_f32_e32 v3, v97, v43
	v_cvt_pk_bf16_f32 v2, v2, v3
	v_mul_f32_e32 v3, v98, v44
	v_mul_f32_e32 v4, v99, v45
	v_cvt_pk_bf16_f32 v3, v3, v4
	v_add_u32_e32 v4, 48, v6
	v_xad_u32 v4, v4, v9, v10
	ds_write_b64 v4, v[2:3] offset:32768
	v_lshlrev_b32_e32 v2, 3, v100
	v_and_b32_e32 v4, 0xc0, v8
	v_lshl_add_u32 v3, v101, 8, v2
	v_and_or_b32 v2, v2, 24, v4
	v_lshlrev_b32_e32 v4, 1, v100
	v_and_b32_e32 v4, 32, v4
	v_and_b32_e32 v3, 0x100, v3
	v_or3_b32 v2, v2, v4, v3
	s_waitcnt lgkmcnt(0)
	s_barrier
	v_add_u32_e32 v3, s28, v2
	ds_read_b64_tr_b16 v[70:71], v3 offset:0
	ds_read_b64_tr_b16 v[72:73], v3 offset:0x800
	ds_read_b64_tr_b16 v[66:67], v3 offset:0x1000
	ds_read_b64_tr_b16 v[68:69], v3 offset:0x1800
	v_add_u32_e32 v6, s29, v2
	ds_read_b64_tr_b16 v[2:3], v6 offset:0
	ds_read_b64_tr_b16 v[4:5], v6 offset:0x800
	ds_read_b64_tr_b16 v[18:19], v6 offset:0x1000
	ds_read_b64_tr_b16 v[20:21], v6 offset:0x1800
	s_waitcnt lgkmcnt(0)
	v_lshlrev_b32_e32 v6, 4, v101
	v_add_u32_e32 v22, s33, v6
	v_add_u32_e32 v23, s46, v6
	v_mfma_f32_32x32x16_bf16 v[2:17], v[2:5], v[70:73], 0
	ds_read_b128 v[34:37], v22
	ds_read_b128 v[38:41], v22 offset:32
	ds_read_b128 v[58:61], v23
	ds_read_b128 v[54:57], v23 offset:32
	ds_read_b128 v[42:45], v22 offset:64
	ds_read_b128 v[50:53], v23 offset:64
	ds_read_b128 v[46:49], v22 offset:96
	ds_read_b128 v[62:65], v23 offset:96
	s_andn2_b64 vcc, exec, s[42:43]
	v_mfma_f32_32x32x16_bf16 v[2:17], v[18:21], v[66:69], v[2:17]
	s_cbranch_vccnz .LBB0_295
	ds_read_b128 v[182:185], v105 offset:8192
	ds_read_b128 v[140:143], v105
	ds_read_b128 v[186:189], v106 offset:8192
	ds_read_b128 v[144:147], v106
	ds_read_b128 v[190:193], v107 offset:8192
	ds_read_b128 v[148:151], v107
	ds_read_b128 v[194:197], v108 offset:8192
	ds_read_b128 v[74:77], v108
	ds_read_b128 v[198:201], v109 offset:8192
	ds_read_b128 v[78:81], v109
	ds_read_b128 v[202:205], v110 offset:8192
	ds_read_b128 v[156:159], v110
	ds_read_b128 v[234:237], v111 offset:8192
	ds_read_b128 v[160:163], v111
	ds_read_b128 v[238:241], v112 offset:8192
	ds_read_b128 v[152:155], v112
	v_cmp_le_i32_e32 vcc, v139, v100
	v_or_b32_e32 v172, 2, v139
	v_or_b32_e32 v173, 3, v139
	v_add_u32_e32 v174, 8, v139
	v_add_u32_e32 v175, 9, v139
	v_add_u32_e32 v176, 10, v139
	v_add_u32_e32 v177, 11, v139
	v_add_u32_e32 v178, 24, v139
	v_add_u32_e32 v179, 25, v139
	v_add_u32_e32 v180, 26, v139
	s_lshl_b32 s56, s7, 5
	s_cmp_gt_i32 s7, 7
	s_cselect_b32 s7, s90, 0xff
	s_sub_i32 s7, s7, s56
	s_and_b64 s[76:77], s[10:11], exec
	s_cselect_b32 s7, s56, s7
	s_add_i32 s76, s7, s3
	s_ashr_i32 s77, s76, 31
	s_lshl_b64 s[76:77], s[76:77], 11
	s_add_u32 s76, s47, s76
	s_addc_u32 s77, s52, s77
	v_add_u32_e32 v164, 16, v139
	v_add_u32_e32 v165, 17, v139
	v_add_u32_e32 v166, 18, v139
	v_add_u32_e32 v167, 19, v139
	s_waitcnt lgkmcnt(14)
	v_mfma_f32_32x32x16_bf16 v[18:33], v[182:185], v[140:143], 0
	s_waitcnt lgkmcnt(12)
	v_mfma_f32_32x32x16_bf16 v[18:33], v[186:189], v[144:147], v[18:33]
	s_waitcnt lgkmcnt(10)
	v_mfma_f32_32x32x16_bf16 v[18:33], v[190:193], v[148:151], v[18:33]
	s_waitcnt lgkmcnt(8)
	v_mfma_f32_32x32x16_bf16 v[18:33], v[194:197], v[74:77], v[18:33]
	s_waitcnt lgkmcnt(6)
	v_mfma_f32_32x32x16_bf16 v[18:33], v[198:201], v[78:81], v[18:33]
	s_waitcnt lgkmcnt(4)
	v_mfma_f32_32x32x16_bf16 v[18:33], v[202:205], v[156:159], v[18:33]
	s_waitcnt lgkmcnt(2)
	v_mfma_f32_32x32x16_bf16 v[18:33], v[234:237], v[160:163], v[18:33]
	s_waitcnt lgkmcnt(0)
	v_mfma_f32_32x32x16_bf16 v[18:33], v[238:241], v[152:155], v[18:33]
	v_add_u32_e32 v242, s27, v105
	ds_read_b128 v[182:185], v242 offset:32768
	v_add_u32_e32 v242, s27, v106
	ds_read_b128 v[186:189], v242 offset:32768
	v_add_u32_e32 v242, s27, v107
	ds_read_b128 v[190:193], v242 offset:32768
	v_add_u32_e32 v242, s27, v108
	ds_read_b128 v[194:197], v242 offset:32768
	v_add_u32_e32 v242, s27, v109
	ds_read_b128 v[198:201], v242 offset:32768
	v_add_u32_e32 v242, s27, v110
	ds_read_b128 v[202:205], v242 offset:32768
	v_add_u32_e32 v242, s27, v111
	ds_read_b128 v[234:237], v242 offset:32768
	v_add_u32_e32 v242, s27, v112
	ds_read_b128 v[238:241], v242 offset:32768
	v_cndmask_b32_e32 v18, 0, v18, vcc
	v_cmp_lt_i32_e32 vcc, v139, v100
	v_add_u32_e32 v139, 27, v139
	s_nop 0
	v_cndmask_b32_e32 v19, 0, v19, vcc
	v_cmp_le_i32_e32 vcc, v172, v100
	v_cvt_pk_bf16_f32 v18, v18, v19
	s_nop 1
	v_cndmask_b32_e32 v20, 0, v20, vcc
	v_cmp_le_i32_e32 vcc, v173, v100
	s_nop 1
	v_cndmask_b32_e32 v21, 0, v21, vcc
	v_cmp_le_i32_e32 vcc, v174, v100
	v_cvt_pk_bf16_f32 v19, v20, v21
	s_nop 1
	v_cndmask_b32_e32 v22, 0, v22, vcc
	v_cmp_le_i32_e32 vcc, v175, v100
	s_nop 1
	v_cndmask_b32_e32 v23, 0, v23, vcc
	v_cmp_le_i32_e32 vcc, v176, v100
	v_cvt_pk_bf16_f32 v20, v22, v23
	s_nop 0
	v_permlane32_swap_b32_e32 v18, v20
	v_cndmask_b32_e32 v24, 0, v24, vcc
	v_cmp_le_i32_e32 vcc, v177, v100
	s_nop 1
	v_cndmask_b32_e32 v25, 0, v25, vcc
	v_cmp_le_i32_e32 vcc, v164, v100
	v_cvt_pk_bf16_f32 v21, v24, v25
	s_nop 0
	v_permlane32_swap_b32_e32 v19, v21
	v_cndmask_b32_e32 v26, 0, v26, vcc
	v_cmp_le_i32_e32 vcc, v165, v100
	s_nop 1
	v_cndmask_b32_e32 v27, 0, v27, vcc
	v_cmp_le_i32_e32 vcc, v166, v100
	v_cvt_pk_bf16_f32 v164, v26, v27
	s_nop 1
	v_cndmask_b32_e32 v28, 0, v28, vcc
	v_cmp_le_i32_e32 vcc, v167, v100
	s_nop 1
	v_cndmask_b32_e32 v29, 0, v29, vcc
	v_cmp_le_i32_e32 vcc, v178, v100
	v_cvt_pk_bf16_f32 v165, v28, v29
	s_nop 1
	v_cndmask_b32_e32 v30, 0, v30, vcc
	v_cmp_le_i32_e32 vcc, v179, v100
	s_nop 1
	v_cndmask_b32_e32 v31, 0, v31, vcc
	v_cmp_le_i32_e32 vcc, v180, v100
	v_cvt_pk_bf16_f32 v166, v30, v31
	s_nop 0
	v_permlane32_swap_b32_e32 v164, v166
	v_cndmask_b32_e32 v32, 0, v32, vcc
	v_cmp_le_i32_e32 vcc, v139, v100
	v_add_u32_e32 v139, s27, v110
	s_nop 0
	v_cndmask_b32_e32 v33, 0, v33, vcc
	v_cvt_pk_bf16_f32 v167, v32, v33
	v_mfma_f32_32x32x16_bf16 v[18:33], v[18:21], v[70:73], 0
	v_permlane32_swap_b32_e32 v165, v167
	s_nop 1
	v_mfma_f32_32x32x16_bf16 v[18:33], v[164:167], v[66:69], v[18:33]
	s_waitcnt lgkmcnt(0)
	v_mfma_f32_32x32x16_bf16 v[18:33], v[140:143], v[182:185], v[18:33]
	v_mul_lo_u32 v140, s53, v101
	v_ashrrev_i32_e32 v141, 31, v140
	v_ashrrev_i32_e32 v101, 31, v100
	v_mfma_f32_32x32x16_bf16 v[18:33], v[144:147], v[186:189], v[18:33]
	v_mfma_f32_32x32x16_bf16 v[18:33], v[148:151], v[190:193], v[18:33]
	v_mfma_f32_32x32x16_bf16 v[18:33], v[74:77], v[194:197], v[18:33]
	v_mfma_f32_32x32x16_bf16 v[18:33], v[78:81], v[198:201], v[18:33]
	v_lshl_add_u64 v[66:67], v[140:141], 2, s[76:77]
	v_lshl_add_u64 v[74:75], v[100:101], 2, v[66:67]
	v_lshl_add_u64 v[76:77], s[62:63], 2, v[74:75]
	v_lshl_add_u64 v[78:79], v[76:77], 0, s[86:87]
	v_lshl_add_u64 v[80:81], v[78:79], 0, s[86:87]
	v_lshl_add_u64 v[100:101], v[80:81], 0, s[50:51]
	v_mfma_f32_32x32x16_bf16 v[18:33], v[156:159], v[202:205], v[18:33]
	v_lshl_add_u64 v[140:141], v[100:101], 0, s[86:87]
	v_mfma_f32_32x32x16_bf16 v[18:33], v[160:163], v[234:237], v[18:33]
	v_lshl_add_u64 v[66:67], v[140:141], 0, s[86:87]
	v_lshl_add_u64 v[68:69], v[66:67], 0, s[86:87]
	v_lshl_add_u64 v[142:143], v[68:69], 0, s[50:51]
	v_lshl_add_u64 v[144:145], v[142:143], 0, s[86:87]
	v_lshl_add_u64 v[146:147], v[144:145], 0, s[86:87]
	v_lshl_add_u64 v[148:149], v[146:147], 0, s[86:87]
	v_lshl_add_u64 v[150:151], v[148:149], 0, s[50:51]
	v_mfma_f32_32x32x16_bf16 v[18:33], v[152:155], v[238:241], v[18:33]
	s_nop 11
	global_store_dword v[74:75], v18, off
	global_store_dword v[76:77], v19, off
	global_store_dword v[78:79], v20, off
	global_store_dword v[80:81], v21, off
	global_store_dword v[100:101], v22, off
	global_store_dword v[140:141], v23, off
	global_store_dword v[66:67], v24, off
	global_store_dword v[68:69], v25, off
	global_store_dword v[142:143], v26, off
	global_store_dword v[144:145], v27, off
	global_store_dword v[146:147], v28, off
	global_store_dword v[148:149], v29, off
	global_store_dword v[150:151], v30, off
	v_lshl_add_u64 v[18:19], v[150:151], 0, s[86:87]
	global_store_dword v[18:19], v31, off
	v_lshl_add_u64 v[18:19], v[18:19], 0, s[86:87]
	global_store_dword v[18:19], v32, off
	v_lshl_add_u64 v[18:19], v[18:19], 0, s[86:87]
	global_store_dword v[18:19], v33, off
	s_branch .LBB0_295
